# attention main loop: DMA issue blocks write m0 directly (no save/restore), loop kept 8-byte aligned
# speedup vs baseline: 1.0097x; 1.0038x over previous
.LBB0_726:
	v_add_u32_e64 v164, s18, v239
	s_add_i32 m0, s38, s30
	s_nop 0
	global_load_lds_dwordx4 v244, s[98:99]
	s_add_i32 m0, s22, s31
	s_nop 0
	global_load_lds_dwordx4 v245, s[98:99]
	s_add_u32 s98, s98, 0x20000
	s_addc_u32 s99, s99, 0
	s_nop 0
	ds_read_b64_tr_b16 v[190:191], v164 offset:24576
	ds_read_b64_tr_b16 v[192:193], v164 offset:25088
	s_waitcnt lgkmcnt(2)
	s_nop 0
	v_mfma_f32_32x32x16_bf16 v[48:63], v[158:161], v[110:113], v[48:63]
	v_add_f32_e32 v114, v80, v81
	v_add_f32_e32 v114, v82, v114
	v_add_f32_e32 v114, v83, v114
	v_add_f32_e32 v114, v84, v114
	v_add_f32_e64 v114, v85, v114
	v_cvt_pk_bf16_f32 v126, v80, v81
	v_cvt_pk_bf16_f32 v127, v82, v83
	ds_read_b64_tr_b16 v[186:187], v164 offset:28672
	ds_read_b64_tr_b16 v[188:189], v164 offset:29184
	v_mfma_f32_32x32x16_bf16 v[32:47], v[146:149], v[110:113], v[32:47]
	v_add_f32_e32 v80, v86, v114
	v_add_f32_e32 v80, v87, v80
	v_add_f32_e32 v80, v88, v80
	v_add_f32_e32 v80, v89, v80
	v_cvt_pk_bf16_f32 v128, v84, v85
	v_cvt_pk_bf16_f32 v129, v86, v87
	ds_read_b64_tr_b16 v[182:183], v164 offset:25600
	ds_read_b64_tr_b16 v[184:185], v164 offset:26112
	v_mfma_f32_32x32x16_bf16 v[48:63], v[154:157], v[106:109], v[48:63]
	v_add_f32_e32 v80, v90, v80
	v_add_f32_e32 v80, v91, v80
	v_add_f32_e32 v80, v92, v80
	v_add_f32_e32 v80, v93, v80
	v_cvt_pk_bf16_f32 v122, v88, v89
	v_cvt_pk_bf16_f32 v123, v90, v91
	ds_read_b64_tr_b16 v[178:179], v164 offset:29696
	ds_read_b64_tr_b16 v[180:181], v164 offset:30208
	v_mfma_f32_32x32x16_bf16 v[32:47], v[142:145], v[106:109], v[32:47]
	v_add_f32_e32 v80, v94, v80
	v_add_f32_e32 v80, v95, v80
	v_add_f32_e32 v80, v64, v80
	v_add_f32_e32 v80, v65, v80
	v_cvt_pk_bf16_f32 v124, v92, v93
	v_cvt_pk_bf16_f32 v125, v94, v95
	ds_read_b64_tr_b16 v[166:167], v164 offset:26624
	ds_read_b64_tr_b16 v[168:169], v164 offset:27136
	v_mfma_f32_32x32x16_bf16 v[48:63], v[150:153], v[102:105], v[48:63]
	v_add_f32_e32 v80, v66, v80
	v_add_f32_e32 v80, v67, v80
	v_add_f32_e32 v80, v68, v80
	v_add_f32_e32 v80, v69, v80
	v_cvt_pk_bf16_f32 v118, v64, v65
	v_cvt_pk_bf16_f32 v119, v66, v67
	ds_read_b64_tr_b16 v[174:175], v164 offset:30720
	ds_read_b64_tr_b16 v[176:177], v164 offset:31232
	v_mfma_f32_32x32x16_bf16 v[32:47], v[138:141], v[102:105], v[32:47]
	v_add_f32_e32 v64, v70, v80
	v_add_f32_e32 v64, v71, v64
	v_add_f32_e32 v64, v72, v64
	v_add_f32_e32 v64, v73, v64
	v_cvt_pk_bf16_f32 v120, v68, v69
	v_cvt_pk_bf16_f32 v121, v70, v71
	ds_read_b64_tr_b16 v[170:171], v164 offset:27648
	ds_read_b64_tr_b16 v[172:173], v164 offset:28160
	v_mfma_f32_32x32x16_bf16 v[48:63], v[134:137], v[98:101], v[48:63]
	v_add_f32_e32 v64, v74, v64
	v_add_f32_e32 v64, v75, v64
	v_add_f32_e32 v64, v76, v64
	v_add_f32_e32 v64, v77, v64
	v_cvt_pk_bf16_f32 v114, v72, v73
	v_cvt_pk_bf16_f32 v115, v74, v75
	ds_read_b64_tr_b16 v[162:163], v164 offset:31744
	ds_read_b64_tr_b16 v[164:165], v164 offset:32256
	v_mfma_f32_32x32x16_bf16 v[32:47], v[130:133], v[98:101], v[32:47]
	v_add_f32_e32 v64, v78, v64
	v_add_f32_e32 v64, v79, v64
	v_add_f32_e64 v224, v240, v64
	v_cvt_pk_bf16_f32 v116, v76, v77
	v_cvt_pk_bf16_f32 v117, v78, v79
	s_waitcnt lgkmcnt(14)
	s_nop 0
	ds_read_b128 v[64:67], v205
	ds_read_b128 v[68:71], v205 offset:32
	ds_read_b128 v[82:85], v205 offset:128
	ds_read_b128 v[86:89], v205 offset:160
	ds_read_b128 v[72:75], v205 offset:64
	ds_read_b128 v[76:79], v205 offset:96
	ds_read_b128 v[90:93], v205 offset:192
	ds_read_b128 v[138:141], v205 offset:224
	v_max_f32_e64 v80, v48, v49
	v_max3_f32 v81, v50, v51, v33
	v_max3_f32 v80, v80, v32, v34
	v_max3_f32 v80, v80, v35, v52
	v_max3_f32 v81, v81, v54, v55
	v_max3_f32 v80, v80, v53, v36
	v_max3_f32 v81, v81, v38, v39
	v_max3_f32 v80, v80, v37, v56
	v_max3_f32 v81, v81, v58, v59
	v_max3_f32 v80, v80, v57, v40
	v_max3_f32 v81, v81, v42, v43
	v_max3_f32 v80, v80, v41, v60
	v_max3_f32 v81, v81, v62, v63
	v_max3_f32 v80, v80, v61, v44
	v_max3_f32 v81, v81, v46, v47
	v_max3_f32 v80, v80, v45, v81
	v_mov_b32_e32 v81, v80
	s_nop 1
	v_permlane32_swap_b32_e32 v80, v81
	v_max_f32_e32 v80, v80, v81
	v_cmp_lt_f32_e32 vcc, s51, v80
	s_cmp_lg_u64 vcc, 0
	s_cselect_b64 s[18:19], -1, 0
	s_cbranch_vccnz .LBB0_734

.LBB0_729:
	s_add_i32 s18, s22, 0x2000
	v_add_u32_e64 v162, s38, v239
	s_cmpk_lg_i32 s22, 0x4000
	s_cselect_b32 s38, s18, 0
	s_add_i32 m0, s22, s30
	s_nop 0
	global_load_lds_dwordx4 v244, s[98:99]
	s_add_i32 m0, s38, s31
	s_nop 0
	global_load_lds_dwordx4 v245, s[98:99]
	s_add_u32 s98, s98, 0x20000
	s_addc_u32 s99, s99, 0
	s_nop 0
	ds_read_b64_tr_b16 v[194:195], v162 offset:24576
	ds_read_b64_tr_b16 v[196:197], v162 offset:25088
	s_waitcnt lgkmcnt(2)
	s_nop 0
	v_mfma_f32_32x32x16_bf16 v[80:95], v[134:137], v[110:113], v[80:95]
	v_add_f32_e32 v114, v48, v49
	v_add_f32_e32 v114, v50, v114
	v_add_f32_e32 v114, v51, v114
	v_add_f32_e32 v114, v52, v114
	v_add_f32_e64 v114, v53, v114
	v_cvt_pk_bf16_f32 v126, v48, v49
	v_cvt_pk_bf16_f32 v127, v50, v51
	ds_read_b64_tr_b16 v[190:191], v162 offset:28672
	ds_read_b64_tr_b16 v[192:193], v162 offset:29184
	v_mfma_f32_32x32x16_bf16 v[64:79], v[130:133], v[110:113], v[64:79]
	v_add_f32_e32 v48, v54, v114
	v_add_f32_e32 v48, v55, v48
	v_add_f32_e32 v48, v56, v48
	v_add_f32_e32 v48, v57, v48
	v_cvt_pk_bf16_f32 v128, v52, v53
	v_cvt_pk_bf16_f32 v129, v54, v55
	ds_read_b64_tr_b16 v[186:187], v162 offset:25600
	ds_read_b64_tr_b16 v[188:189], v162 offset:26112
	v_mfma_f32_32x32x16_bf16 v[80:95], v[146:149], v[106:109], v[80:95]
	v_add_f32_e32 v48, v58, v48
	v_add_f32_e32 v48, v59, v48
	v_add_f32_e32 v48, v60, v48
	v_add_f32_e32 v48, v61, v48
	v_cvt_pk_bf16_f32 v122, v56, v57
	v_cvt_pk_bf16_f32 v123, v58, v59
	ds_read_b64_tr_b16 v[138:139], v162 offset:29696
	ds_read_b64_tr_b16 v[140:141], v162 offset:30208
	v_mfma_f32_32x32x16_bf16 v[64:79], v[142:145], v[106:109], v[64:79]
	v_add_f32_e32 v48, v62, v48
	v_add_f32_e32 v48, v63, v48
	v_add_f32_e32 v48, v32, v48
	v_add_f32_e32 v48, v33, v48
	v_cvt_pk_bf16_f32 v124, v60, v61
	v_cvt_pk_bf16_f32 v125, v62, v63
	ds_read_b64_tr_b16 v[182:183], v162 offset:26624
	ds_read_b64_tr_b16 v[184:185], v162 offset:27136
	v_mfma_f32_32x32x16_bf16 v[80:95], v[158:161], v[102:105], v[80:95]
	v_add_f32_e32 v48, v34, v48
	v_add_f32_e32 v48, v35, v48
	v_add_f32_e32 v48, v36, v48
	v_add_f32_e32 v48, v37, v48
	v_cvt_pk_bf16_f32 v118, v32, v33
	v_cvt_pk_bf16_f32 v119, v34, v35
	ds_read_b64_tr_b16 v[178:179], v162 offset:30720
	ds_read_b64_tr_b16 v[180:181], v162 offset:31232
	v_mfma_f32_32x32x16_bf16 v[64:79], v[154:157], v[102:105], v[64:79]
	v_add_f32_e32 v32, v38, v48
	v_add_f32_e32 v32, v39, v32
	v_add_f32_e32 v32, v40, v32
	v_add_f32_e32 v32, v41, v32
	v_cvt_pk_bf16_f32 v120, v36, v37
	v_cvt_pk_bf16_f32 v121, v38, v39
	ds_read_b64_tr_b16 v[174:175], v162 offset:27648
	ds_read_b64_tr_b16 v[176:177], v162 offset:28160
	v_mfma_f32_32x32x16_bf16 v[80:95], v[166:169], v[98:101], v[80:95]
	v_add_f32_e32 v32, v42, v32
	v_add_f32_e32 v32, v43, v32
	v_add_f32_e32 v32, v44, v32
	v_add_f32_e32 v32, v45, v32
	v_cvt_pk_bf16_f32 v114, v40, v41
	v_cvt_pk_bf16_f32 v115, v42, v43
	ds_read_b64_tr_b16 v[170:171], v162 offset:31744
	ds_read_b64_tr_b16 v[172:173], v162 offset:32256
	v_mfma_f32_32x32x16_bf16 v[64:79], v[150:153], v[98:101], v[64:79]
	v_add_f32_e32 v32, v46, v32
	v_add_f32_e32 v32, v47, v32
	v_add_f32_e64 v240, v224, v32
	v_cvt_pk_bf16_f32 v116, v44, v45
	v_cvt_pk_bf16_f32 v117, v46, v47
	s_waitcnt lgkmcnt(14)
	s_nop 0
	ds_read_b128 v[32:35], v205 offset:256
	ds_read_b128 v[36:39], v205 offset:288
	ds_read_b128 v[50:53], v205 offset:384
	ds_read_b128 v[54:57], v205 offset:416
	ds_read_b128 v[40:43], v205 offset:320
	ds_read_b128 v[44:47], v205 offset:352
	ds_read_b128 v[58:61], v205 offset:448
	ds_read_b128 v[162:165], v205 offset:480
	v_max_f32_e64 v48, v80, v81
	v_max3_f32 v49, v82, v83, v65
	v_max3_f32 v48, v48, v64, v66
	v_max3_f32 v48, v48, v67, v84
	v_max3_f32 v49, v49, v86, v87
	v_max3_f32 v48, v48, v85, v68
	v_max3_f32 v49, v49, v70, v71
	v_max3_f32 v48, v48, v69, v88
	v_max3_f32 v49, v49, v90, v91
	v_max3_f32 v48, v48, v89, v72
	v_max3_f32 v49, v49, v74, v75
	v_max3_f32 v48, v48, v73, v92
	v_max3_f32 v49, v49, v94, v95
	v_max3_f32 v48, v48, v93, v76
	v_max3_f32 v49, v49, v78, v79
	v_max3_f32 v48, v48, v77, v49
	v_mov_b32_e32 v49, v48
	s_nop 1
	v_permlane32_swap_b32_e32 v48, v49
	v_max_f32_e32 v48, v48, v49
	v_cmp_lt_f32_e32 vcc, s51, v48
	s_cmp_lg_u64 vcc, 0
	s_cselect_b64 s[18:19], -1, 0
	s_cbranch_vccnz .LBB0_737
